# gate unit selection stage: 32 dependent ds_read_b32+wait steps replaced by 8 wide LDS reads up front (v13..v44); on top of the kmean/gate-staging/barrier/QK-prefetch version
# baseline (speedup 1.0000x reference)
.LBB0_501:
	s_or_b64 exec, exec, s[8:9]
	s_movk_i32 s0, 0x100
	v_cmp_gt_i32_e64 s[0:1], s0, v6
	s_waitcnt lgkmcnt(0)
	s_barrier
	s_and_saveexec_b64 s[8:9], s[0:1]
	s_cbranch_execz .LBB0_567
	v_and_b32_e32 v8, 0xffffffe0, v6
	v_lshl_add_u32 v9, v8, 2, 0
	ds_read_b128 v[14:17], v9
	ds_read_b128 v[18:21], v9 offset:16
	ds_read_b128 v[22:25], v9 offset:32
	ds_read_b128 v[26:29], v9 offset:48
	ds_read_b128 v[30:33], v9 offset:64
	ds_read_b128 v[34:37], v9 offset:80
	ds_read_b128 v[38:41], v9 offset:96
	ds_read_b64 v[42:43], v9 offset:112
	ds_read_b32 v44, v9 offset:120
	ds_read_b32 v13, v9 offset:124
	s_waitcnt lgkmcnt(0)
	v_mov_b32_e32 v11, v14
	v_lshlrev_b32_e64 v5, v72, 1
	v_lshlrev_b32_e64 v2, v72, -1
	v_mov_b32_e32 v7, 0
	v_not_b32_e32 v2, v2
	v_and_b32_e32 v12, v11, v5
	v_cmp_ne_u32_e64 s[0:1], 0, v12
	v_lshlrev_b32_e32 v8, 4, v8
	s_and_saveexec_b64 s[10:11], s[0:1]
	s_cbranch_execz .LBB0_504
	v_and_b32_e32 v7, v11, v2
	v_bcnt_u32_b32 v7, v7, 0
	v_lshlrev_b32_e32 v7, 2, v7
	v_add3_u32 v7, 0, v8, v7
	ds_write_b32 v7, v3 offset:3200
	v_mov_b32_e32 v7, 1
.LBB0_504:
	s_or_b64 exec, exec, s[10:11]
	v_mov_b32_e32 v11, v15
	v_and_b32_e32 v12, v11, v5
	v_cmp_ne_u32_e64 s[0:1], 0, v12
	s_and_saveexec_b64 s[10:11], s[0:1]
	s_cbranch_execz .LBB0_506
	v_and_b32_e32 v11, v11, v2
	v_bcnt_u32_b32 v11, v11, 0
	v_lshlrev_b32_e32 v11, 2, v11
	v_add3_u32 v11, 0, v8, v11
	v_add_u32_e32 v12, 1, v7
	ds_write_b32 v11, v7 offset:3216
	v_mov_b32_e32 v7, v12
.LBB0_506:
	s_or_b64 exec, exec, s[10:11]
	v_mov_b32_e32 v11, v16
	v_and_b32_e32 v12, v11, v5
	v_cmp_ne_u32_e64 s[0:1], 0, v12
	s_and_saveexec_b64 s[10:11], s[0:1]
	s_cbranch_execz .LBB0_508
	v_and_b32_e32 v11, v11, v2
	v_bcnt_u32_b32 v11, v11, 0
	v_lshlrev_b32_e32 v11, 2, v11
	v_add3_u32 v11, 0, v8, v11
	v_add_u32_e32 v12, 1, v7
	ds_write_b32 v11, v7 offset:3232
	v_mov_b32_e32 v7, v12
.LBB0_508:
	s_or_b64 exec, exec, s[10:11]
	v_mov_b32_e32 v11, v17
	v_and_b32_e32 v12, v11, v5
	v_cmp_ne_u32_e64 s[0:1], 0, v12
	s_and_saveexec_b64 s[10:11], s[0:1]
	s_cbranch_execz .LBB0_510
	v_and_b32_e32 v11, v11, v2
	v_bcnt_u32_b32 v11, v11, 0
	v_lshlrev_b32_e32 v11, 2, v11
	v_add3_u32 v11, 0, v8, v11
	v_add_u32_e32 v12, 1, v7
	ds_write_b32 v11, v7 offset:3248
	v_mov_b32_e32 v7, v12
.LBB0_510:
	s_or_b64 exec, exec, s[10:11]
	v_mov_b32_e32 v11, v18
	v_and_b32_e32 v12, v11, v5
	v_cmp_ne_u32_e64 s[0:1], 0, v12
	s_and_saveexec_b64 s[10:11], s[0:1]
	s_cbranch_execz .LBB0_512
	v_and_b32_e32 v11, v11, v2
	v_bcnt_u32_b32 v11, v11, 0
	v_lshlrev_b32_e32 v11, 2, v11
	v_add3_u32 v11, 0, v8, v11
	v_add_u32_e32 v12, 1, v7
	ds_write_b32 v11, v7 offset:3264
	v_mov_b32_e32 v7, v12
.LBB0_512:
	s_or_b64 exec, exec, s[10:11]
	v_mov_b32_e32 v11, v19
	v_and_b32_e32 v12, v11, v5
	v_cmp_ne_u32_e64 s[0:1], 0, v12
	s_and_saveexec_b64 s[10:11], s[0:1]
	s_cbranch_execz .LBB0_514
	v_and_b32_e32 v11, v11, v2
	v_bcnt_u32_b32 v11, v11, 0
	v_lshlrev_b32_e32 v11, 2, v11
	v_add3_u32 v11, 0, v8, v11
	v_add_u32_e32 v12, 1, v7
	ds_write_b32 v11, v7 offset:3280
	v_mov_b32_e32 v7, v12
.LBB0_514:
	s_or_b64 exec, exec, s[10:11]
	v_mov_b32_e32 v11, v20
	v_and_b32_e32 v12, v11, v5
	v_cmp_ne_u32_e64 s[0:1], 0, v12
	s_and_saveexec_b64 s[10:11], s[0:1]
	s_cbranch_execz .LBB0_516
	v_and_b32_e32 v11, v11, v2
	v_bcnt_u32_b32 v11, v11, 0
	v_lshlrev_b32_e32 v11, 2, v11
	v_add3_u32 v11, 0, v8, v11
	v_add_u32_e32 v12, 1, v7
	ds_write_b32 v11, v7 offset:3296
	v_mov_b32_e32 v7, v12
.LBB0_516:
	s_or_b64 exec, exec, s[10:11]
	v_mov_b32_e32 v11, v21
	v_and_b32_e32 v12, v11, v5
	v_cmp_ne_u32_e64 s[0:1], 0, v12
	s_and_saveexec_b64 s[10:11], s[0:1]
	s_cbranch_execz .LBB0_518
	v_and_b32_e32 v11, v11, v2
	v_bcnt_u32_b32 v11, v11, 0
	v_lshlrev_b32_e32 v11, 2, v11
	v_add3_u32 v11, 0, v8, v11
	v_add_u32_e32 v12, 1, v7
	ds_write_b32 v11, v7 offset:3312
	v_mov_b32_e32 v7, v12
.LBB0_518:
	s_or_b64 exec, exec, s[10:11]
	v_mov_b32_e32 v11, v22
	v_and_b32_e32 v12, v11, v5
	v_cmp_ne_u32_e64 s[0:1], 0, v12
	s_and_saveexec_b64 s[10:11], s[0:1]
	s_cbranch_execz .LBB0_520
	v_and_b32_e32 v11, v11, v2
	v_bcnt_u32_b32 v11, v11, 0
	v_lshlrev_b32_e32 v11, 2, v11
	v_add3_u32 v11, 0, v8, v11
	v_add_u32_e32 v12, 1, v7
	ds_write_b32 v11, v7 offset:3328
	v_mov_b32_e32 v7, v12
.LBB0_520:
	s_or_b64 exec, exec, s[10:11]
	v_mov_b32_e32 v11, v23
	v_and_b32_e32 v12, v11, v5
	v_cmp_ne_u32_e64 s[0:1], 0, v12
	s_and_saveexec_b64 s[10:11], s[0:1]
	s_cbranch_execz .LBB0_522
	v_and_b32_e32 v11, v11, v2
	v_bcnt_u32_b32 v11, v11, 0
	v_lshlrev_b32_e32 v11, 2, v11
	v_add3_u32 v11, 0, v8, v11
	v_add_u32_e32 v12, 1, v7
	ds_write_b32 v11, v7 offset:3344
	v_mov_b32_e32 v7, v12
.LBB0_522:
	s_or_b64 exec, exec, s[10:11]
	v_mov_b32_e32 v11, v24
	v_and_b32_e32 v12, v11, v5
	v_cmp_ne_u32_e64 s[0:1], 0, v12
	s_and_saveexec_b64 s[10:11], s[0:1]
	s_cbranch_execz .LBB0_524
	v_and_b32_e32 v11, v11, v2
	v_bcnt_u32_b32 v11, v11, 0
	v_lshlrev_b32_e32 v11, 2, v11
	v_add3_u32 v11, 0, v8, v11
	v_add_u32_e32 v12, 1, v7
	ds_write_b32 v11, v7 offset:3360
	v_mov_b32_e32 v7, v12
.LBB0_524:
	s_or_b64 exec, exec, s[10:11]
	v_mov_b32_e32 v11, v25
	v_and_b32_e32 v12, v11, v5
	v_cmp_ne_u32_e64 s[0:1], 0, v12
	s_and_saveexec_b64 s[10:11], s[0:1]
	s_cbranch_execz .LBB0_526
	v_and_b32_e32 v11, v11, v2
	v_bcnt_u32_b32 v11, v11, 0
	v_lshlrev_b32_e32 v11, 2, v11
	v_add3_u32 v11, 0, v8, v11
	v_add_u32_e32 v12, 1, v7
	ds_write_b32 v11, v7 offset:3376
	v_mov_b32_e32 v7, v12
.LBB0_526:
	s_or_b64 exec, exec, s[10:11]
	v_mov_b32_e32 v11, v26
	v_and_b32_e32 v12, v11, v5
	v_cmp_ne_u32_e64 s[0:1], 0, v12
	s_and_saveexec_b64 s[10:11], s[0:1]
	s_cbranch_execz .LBB0_528
	v_and_b32_e32 v11, v11, v2
	v_bcnt_u32_b32 v11, v11, 0
	v_lshlrev_b32_e32 v11, 2, v11
	v_add3_u32 v11, 0, v8, v11
	v_add_u32_e32 v12, 1, v7
	ds_write_b32 v11, v7 offset:3392
	v_mov_b32_e32 v7, v12
.LBB0_528:
	s_or_b64 exec, exec, s[10:11]
	v_mov_b32_e32 v11, v27
	v_and_b32_e32 v12, v11, v5
	v_cmp_ne_u32_e64 s[0:1], 0, v12
	s_and_saveexec_b64 s[10:11], s[0:1]
	s_cbranch_execz .LBB0_530
	v_and_b32_e32 v11, v11, v2
	v_bcnt_u32_b32 v11, v11, 0
	v_lshlrev_b32_e32 v11, 2, v11
	v_add3_u32 v11, 0, v8, v11
	v_add_u32_e32 v12, 1, v7
	ds_write_b32 v11, v7 offset:3408
	v_mov_b32_e32 v7, v12
.LBB0_530:
	s_or_b64 exec, exec, s[10:11]
	v_mov_b32_e32 v11, v28
	v_and_b32_e32 v12, v11, v5
	v_cmp_ne_u32_e64 s[0:1], 0, v12
	s_and_saveexec_b64 s[10:11], s[0:1]
	s_cbranch_execz .LBB0_532
	v_and_b32_e32 v11, v11, v2
	v_bcnt_u32_b32 v11, v11, 0
	v_lshlrev_b32_e32 v11, 2, v11
	v_add3_u32 v11, 0, v8, v11
	v_add_u32_e32 v12, 1, v7
	ds_write_b32 v11, v7 offset:3424
	v_mov_b32_e32 v7, v12
.LBB0_532:
	s_or_b64 exec, exec, s[10:11]
	v_mov_b32_e32 v11, v29
	v_and_b32_e32 v12, v11, v5
	v_cmp_ne_u32_e64 s[0:1], 0, v12
	s_and_saveexec_b64 s[10:11], s[0:1]
	s_cbranch_execz .LBB0_534
	v_and_b32_e32 v11, v11, v2
	v_bcnt_u32_b32 v11, v11, 0
	v_lshlrev_b32_e32 v11, 2, v11
	v_add3_u32 v11, 0, v8, v11
	v_add_u32_e32 v12, 1, v7
	ds_write_b32 v11, v7 offset:3440
	v_mov_b32_e32 v7, v12
.LBB0_534:
	s_or_b64 exec, exec, s[10:11]
	v_mov_b32_e32 v11, v30
	v_and_b32_e32 v12, v11, v5
	v_cmp_ne_u32_e64 s[0:1], 0, v12
	s_and_saveexec_b64 s[10:11], s[0:1]
	s_cbranch_execz .LBB0_536
	v_and_b32_e32 v11, v11, v2
	v_bcnt_u32_b32 v11, v11, 0
	v_lshlrev_b32_e32 v11, 2, v11
	v_add3_u32 v11, 0, v8, v11
	v_add_u32_e32 v12, 1, v7
	ds_write_b32 v11, v7 offset:3456
	v_mov_b32_e32 v7, v12
.LBB0_536:
	s_or_b64 exec, exec, s[10:11]
	v_mov_b32_e32 v11, v31
	v_and_b32_e32 v12, v11, v5
	v_cmp_ne_u32_e64 s[0:1], 0, v12
	s_and_saveexec_b64 s[10:11], s[0:1]
	s_cbranch_execz .LBB0_538
	v_and_b32_e32 v11, v11, v2
	v_bcnt_u32_b32 v11, v11, 0
	v_lshlrev_b32_e32 v11, 2, v11
	v_add3_u32 v11, 0, v8, v11
	v_add_u32_e32 v12, 1, v7
	ds_write_b32 v11, v7 offset:3472
	v_mov_b32_e32 v7, v12
.LBB0_538:
	s_or_b64 exec, exec, s[10:11]
	v_mov_b32_e32 v11, v32
	v_and_b32_e32 v12, v11, v5
	v_cmp_ne_u32_e64 s[0:1], 0, v12
	s_and_saveexec_b64 s[10:11], s[0:1]
	s_cbranch_execz .LBB0_540
	v_and_b32_e32 v11, v11, v2
	v_bcnt_u32_b32 v11, v11, 0
	v_lshlrev_b32_e32 v11, 2, v11
	v_add3_u32 v11, 0, v8, v11
	v_add_u32_e32 v12, 1, v7
	ds_write_b32 v11, v7 offset:3488
	v_mov_b32_e32 v7, v12
.LBB0_540:
	s_or_b64 exec, exec, s[10:11]
	v_mov_b32_e32 v11, v33
	v_and_b32_e32 v12, v11, v5
	v_cmp_ne_u32_e64 s[0:1], 0, v12
	s_and_saveexec_b64 s[10:11], s[0:1]
	s_cbranch_execz .LBB0_542
	v_and_b32_e32 v11, v11, v2
	v_bcnt_u32_b32 v11, v11, 0
	v_lshlrev_b32_e32 v11, 2, v11
	v_add3_u32 v11, 0, v8, v11
	v_add_u32_e32 v12, 1, v7
	ds_write_b32 v11, v7 offset:3504
	v_mov_b32_e32 v7, v12
.LBB0_542:
	s_or_b64 exec, exec, s[10:11]
	v_mov_b32_e32 v11, v34
	v_and_b32_e32 v12, v11, v5
	v_cmp_ne_u32_e64 s[0:1], 0, v12
	s_and_saveexec_b64 s[10:11], s[0:1]
	s_cbranch_execz .LBB0_544
	v_and_b32_e32 v11, v11, v2
	v_bcnt_u32_b32 v11, v11, 0
	v_lshlrev_b32_e32 v11, 2, v11
	v_add3_u32 v11, 0, v8, v11
	v_add_u32_e32 v12, 1, v7
	ds_write_b32 v11, v7 offset:3520
	v_mov_b32_e32 v7, v12
.LBB0_544:
	s_or_b64 exec, exec, s[10:11]
	v_mov_b32_e32 v11, v35
	v_and_b32_e32 v12, v11, v5
	v_cmp_ne_u32_e64 s[0:1], 0, v12
	s_and_saveexec_b64 s[10:11], s[0:1]
	s_cbranch_execz .LBB0_546
	v_and_b32_e32 v11, v11, v2
	v_bcnt_u32_b32 v11, v11, 0
	v_lshlrev_b32_e32 v11, 2, v11
	v_add3_u32 v11, 0, v8, v11
	v_add_u32_e32 v12, 1, v7
	ds_write_b32 v11, v7 offset:3536
	v_mov_b32_e32 v7, v12
.LBB0_546:
	s_or_b64 exec, exec, s[10:11]
	v_mov_b32_e32 v11, v36
	v_and_b32_e32 v12, v11, v5
	v_cmp_ne_u32_e64 s[0:1], 0, v12
	s_and_saveexec_b64 s[10:11], s[0:1]
	s_cbranch_execz .LBB0_548
	v_and_b32_e32 v11, v11, v2
	v_bcnt_u32_b32 v11, v11, 0
	v_lshlrev_b32_e32 v11, 2, v11
	v_add3_u32 v11, 0, v8, v11
	v_add_u32_e32 v12, 1, v7
	ds_write_b32 v11, v7 offset:3552
	v_mov_b32_e32 v7, v12
.LBB0_548:
	s_or_b64 exec, exec, s[10:11]
	v_mov_b32_e32 v11, v37
	v_and_b32_e32 v12, v11, v5
	v_cmp_ne_u32_e64 s[0:1], 0, v12
	s_and_saveexec_b64 s[10:11], s[0:1]
	s_cbranch_execz .LBB0_550
	v_and_b32_e32 v11, v11, v2
	v_bcnt_u32_b32 v11, v11, 0
	v_lshlrev_b32_e32 v11, 2, v11
	v_add3_u32 v11, 0, v8, v11
	v_add_u32_e32 v12, 1, v7
	ds_write_b32 v11, v7 offset:3568
	v_mov_b32_e32 v7, v12
.LBB0_550:
	s_or_b64 exec, exec, s[10:11]
	v_mov_b32_e32 v11, v38
	v_and_b32_e32 v12, v11, v5
	v_cmp_ne_u32_e64 s[0:1], 0, v12
	s_and_saveexec_b64 s[10:11], s[0:1]
	s_cbranch_execz .LBB0_552
	v_and_b32_e32 v11, v11, v2
	v_bcnt_u32_b32 v11, v11, 0
	v_lshlrev_b32_e32 v11, 2, v11
	v_add3_u32 v11, 0, v8, v11
	v_add_u32_e32 v12, 1, v7
	ds_write_b32 v11, v7 offset:3584
	v_mov_b32_e32 v7, v12
.LBB0_552:
	s_or_b64 exec, exec, s[10:11]
	v_mov_b32_e32 v11, v39
	v_and_b32_e32 v12, v11, v5
	v_cmp_ne_u32_e64 s[0:1], 0, v12
	s_and_saveexec_b64 s[10:11], s[0:1]
	s_cbranch_execz .LBB0_554
	v_and_b32_e32 v11, v11, v2
	v_bcnt_u32_b32 v11, v11, 0
	v_lshlrev_b32_e32 v11, 2, v11
	v_add3_u32 v11, 0, v8, v11
	v_add_u32_e32 v12, 1, v7
	ds_write_b32 v11, v7 offset:3600
	v_mov_b32_e32 v7, v12
.LBB0_554:
	s_or_b64 exec, exec, s[10:11]
	v_mov_b32_e32 v11, v40
	v_and_b32_e32 v12, v11, v5
	v_cmp_ne_u32_e64 s[0:1], 0, v12
	s_and_saveexec_b64 s[10:11], s[0:1]
	s_cbranch_execz .LBB0_556
	v_and_b32_e32 v11, v11, v2
	v_bcnt_u32_b32 v11, v11, 0
	v_lshlrev_b32_e32 v11, 2, v11
	v_add3_u32 v11, 0, v8, v11
	v_add_u32_e32 v12, 1, v7
	ds_write_b32 v11, v7 offset:3616
	v_mov_b32_e32 v7, v12
.LBB0_556:
	s_or_b64 exec, exec, s[10:11]
	v_mov_b32_e32 v11, v41
	v_and_b32_e32 v12, v11, v5
	v_cmp_ne_u32_e64 s[0:1], 0, v12
	s_and_saveexec_b64 s[10:11], s[0:1]
	s_cbranch_execz .LBB0_558
	v_and_b32_e32 v11, v11, v2
	v_bcnt_u32_b32 v11, v11, 0
	v_lshlrev_b32_e32 v11, 2, v11
	v_add3_u32 v11, 0, v8, v11
	v_add_u32_e32 v12, 1, v7
	ds_write_b32 v11, v7 offset:3632
	v_mov_b32_e32 v7, v12
.LBB0_558:
	s_or_b64 exec, exec, s[10:11]
	v_mov_b32_e32 v11, v42
	v_and_b32_e32 v12, v11, v5
	v_cmp_ne_u32_e64 s[0:1], 0, v12
	s_and_saveexec_b64 s[10:11], s[0:1]
	s_cbranch_execz .LBB0_560
	v_and_b32_e32 v11, v11, v2
	v_bcnt_u32_b32 v11, v11, 0
	v_lshlrev_b32_e32 v11, 2, v11
	v_add3_u32 v11, 0, v8, v11
	v_add_u32_e32 v12, 1, v7
	ds_write_b32 v11, v7 offset:3648
	v_mov_b32_e32 v7, v12
.LBB0_560:
	s_or_b64 exec, exec, s[10:11]
	v_mov_b32_e32 v11, v43
	v_and_b32_e32 v12, v11, v5
	v_cmp_ne_u32_e64 s[0:1], 0, v12
	s_and_saveexec_b64 s[10:11], s[0:1]
	s_cbranch_execz .LBB0_562
	v_and_b32_e32 v11, v11, v2
	v_bcnt_u32_b32 v11, v11, 0
	v_lshlrev_b32_e32 v11, 2, v11
	v_add3_u32 v11, 0, v8, v11
	v_add_u32_e32 v12, 1, v7
	ds_write_b32 v11, v7 offset:3664
	v_mov_b32_e32 v7, v12
.LBB0_562:
	s_or_b64 exec, exec, s[10:11]
	v_mov_b32_e32 v9, v44
	v_and_b32_e32 v11, v9, v5
	v_cmp_ne_u32_e64 s[0:1], 0, v11
	s_and_saveexec_b64 s[10:11], s[0:1]
	s_cbranch_execz .LBB0_564
	v_and_b32_e32 v9, v9, v2
	v_bcnt_u32_b32 v9, v9, 0
	v_lshlrev_b32_e32 v9, 2, v9
	v_add3_u32 v8, 0, v8, v9
	v_add_u32_e32 v9, 1, v7
	ds_write_b32 v8, v7 offset:3680
	v_mov_b32_e32 v7, v9
.LBB0_564:
	s_or_b64 exec, exec, s[10:11]
	v_or_b32_e32 v8, 31, v6
	v_lshl_add_u32 v9, v8, 2, 0
	v_mov_b32_e32 v9, v13
	v_and_b32_e32 v5, v9, v5
	v_cmp_ne_u32_e64 s[0:1], 0, v5
	s_and_saveexec_b64 s[10:11], s[0:1]
	s_cbranch_execz .LBB0_566
	v_and_b32_e32 v2, v9, v2
	v_bcnt_u32_b32 v2, v2, 0
	v_lshlrev_b32_e32 v5, 4, v8
	v_lshlrev_b32_e32 v2, 2, v2
	v_add3_u32 v2, 0, v5, v2
	v_add_u32_e32 v5, 1, v7
	ds_write_b32 v2, v7 offset:3200
	v_mov_b32_e32 v7, v5
